# P1 conversion slot of odd workgroups (before their GEMM) as hand-written 2-deep loop with items rotated across the two row blocks; even workgroups keep compiler loop
# baseline (speedup 1.0000x reference)
.LBB0_141:
	s_add_i32 s33, s52, s53
	v_readlane_b32 s0, v255, 4
	s_bitcmp0_b32 s0, 0
	s_cselect_b64 s[54:55], -1, 0
	s_and_b64 vcc, exec, s[54:55]
	s_cbranch_vccnz .LBB0_177
	s_waitcnt vmcnt(0)
	v_readlane_b32 s2, v255, 28
	s_mul_i32 s11, s96, 0xa0
	s_add_i32 s11, s11, s2
	v_mbcnt_lo_u32_b32 v146, -1, 0
	v_mbcnt_hi_u32_b32 v146, -1, v146
	v_lshrrev_b32_e32 v147, 3, v146
	v_and_b32_e32 v146, 7, v146
	v_lshlrev_b32_e32 v144, 18, v147
	v_lshl_or_b32 v144, v146, 4, v144
	v_lshlrev_b32_e32 v145, 13, v146
	v_lshl_or_b32 v145, v147, 4, v145
	s_mov_b32 s36, 0x44000000
	s_add_i32 s1, s11, 0
	s_and_b32 s2, s1, 1
	s_lshl_b32 s2, s2, 7
	s_and_b32 s4, s1, 0xfe
	s_lshr_b32 s4, s4, 1
	s_andn2_b32 s1, s1, 0xff
	s_or_b32 s1, s1, s2
	s_or_b32 s1, s1, s4
	s_lshr_b32 s2, s1, 11
	s_and_b32 s4, s1, 0x7ff
	s_lshr_b32 s5, s4, 7
	s_and_b32 s4, s4, 127
	s_lshl_b32 s12, s2, 25
	s_lshl_b32 s13, s5, 21
	s_add_i32 s12, s12, s13
	s_lshl_b32 s13, s4, 7
	s_add_i32 s12, s12, s13
	s_add_u32 s6, s66, s12
	s_addc_u32 s7, s67, 0
	global_load_dwordx4 v[0:3], v144, s[6:7] sc1 nt
	s_add_u32 s8, s6, 0x4000
	s_addc_u32 s9, s7, 0
	global_load_dwordx4 v[4:7], v144, s[8:9] sc1 nt
	s_add_u32 s8, s6, 0x8000
	s_addc_u32 s9, s7, 0
	global_load_dwordx4 v[8:11], v144, s[8:9] sc1 nt
	s_add_u32 s8, s6, 0xc000
	s_addc_u32 s9, s7, 0
	global_load_dwordx4 v[12:15], v144, s[8:9] sc1 nt
	s_add_u32 s8, s6, 0x10000
	s_addc_u32 s9, s7, 0
	global_load_dwordx4 v[16:19], v144, s[8:9] sc1 nt
	s_add_u32 s8, s6, 0x14000
	s_addc_u32 s9, s7, 0
	global_load_dwordx4 v[20:23], v144, s[8:9] sc1 nt
	s_add_u32 s8, s6, 0x18000
	s_addc_u32 s9, s7, 0
	global_load_dwordx4 v[24:27], v144, s[8:9] sc1 nt
	s_add_u32 s8, s6, 0x1c000
	s_addc_u32 s9, s7, 0
	global_load_dwordx4 v[28:31], v144, s[8:9] sc1 nt
	s_add_u32 s8, s6, 0x20000
	s_addc_u32 s9, s7, 0
	global_load_dwordx4 v[32:35], v144, s[8:9] sc1 nt
	s_add_u32 s8, s6, 0x24000
	s_addc_u32 s9, s7, 0
	global_load_dwordx4 v[36:39], v144, s[8:9] sc1 nt
	s_add_u32 s8, s6, 0x28000
	s_addc_u32 s9, s7, 0
	global_load_dwordx4 v[40:43], v144, s[8:9] sc1 nt
	s_add_u32 s8, s6, 0x2c000
	s_addc_u32 s9, s7, 0
	global_load_dwordx4 v[44:47], v144, s[8:9] sc1 nt
	s_add_u32 s8, s6, 0x30000
	s_addc_u32 s9, s7, 0
	global_load_dwordx4 v[48:51], v144, s[8:9] sc1 nt
	s_add_u32 s8, s6, 0x34000
	s_addc_u32 s9, s7, 0
	global_load_dwordx4 v[52:55], v144, s[8:9] sc1 nt
	s_add_u32 s8, s6, 0x38000
	s_addc_u32 s9, s7, 0
	global_load_dwordx4 v[56:59], v144, s[8:9] sc1 nt
	s_add_u32 s8, s6, 0x3c000
	s_addc_u32 s9, s7, 0
	global_load_dwordx4 v[60:63], v144, s[8:9] sc1 nt
	s_add_i32 s1, s11, 8
	s_and_b32 s2, s1, 1
	s_lshl_b32 s2, s2, 7
	s_and_b32 s4, s1, 0xfe
	s_lshr_b32 s4, s4, 1
	s_andn2_b32 s1, s1, 0xff
	s_or_b32 s1, s1, s2
	s_or_b32 s1, s1, s4
	s_lshr_b32 s2, s1, 11
	s_and_b32 s4, s1, 0x7ff
	s_lshr_b32 s5, s4, 7
	s_and_b32 s4, s4, 127
	s_lshl_b32 s12, s2, 25
	s_lshl_b32 s13, s5, 21
	s_add_i32 s12, s12, s13
	s_lshl_b32 s13, s4, 7
	s_add_i32 s12, s12, s13
	s_add_u32 s6, s66, s12
	s_addc_u32 s7, s67, 0
	global_load_dwordx4 v[64:67], v144, s[6:7] sc1 nt
	s_add_u32 s8, s6, 0x4000
	s_addc_u32 s9, s7, 0
	global_load_dwordx4 v[68:71], v144, s[8:9] sc1 nt
	s_add_u32 s8, s6, 0x8000
	s_addc_u32 s9, s7, 0
	global_load_dwordx4 v[72:75], v144, s[8:9] sc1 nt
	s_add_u32 s8, s6, 0xc000
	s_addc_u32 s9, s7, 0
	global_load_dwordx4 v[76:79], v144, s[8:9] sc1 nt
	s_add_u32 s8, s6, 0x10000
	s_addc_u32 s9, s7, 0
	global_load_dwordx4 v[80:83], v144, s[8:9] sc1 nt
	s_add_u32 s8, s6, 0x14000
	s_addc_u32 s9, s7, 0
	global_load_dwordx4 v[84:87], v144, s[8:9] sc1 nt
	s_add_u32 s8, s6, 0x18000
	s_addc_u32 s9, s7, 0
	global_load_dwordx4 v[88:91], v144, s[8:9] sc1 nt
	s_add_u32 s8, s6, 0x1c000
	s_addc_u32 s9, s7, 0
	global_load_dwordx4 v[92:95], v144, s[8:9] sc1 nt
	s_add_u32 s8, s6, 0x20000
	s_addc_u32 s9, s7, 0
	global_load_dwordx4 v[96:99], v144, s[8:9] sc1 nt
	s_add_u32 s8, s6, 0x24000
	s_addc_u32 s9, s7, 0
	global_load_dwordx4 v[100:103], v144, s[8:9] sc1 nt
	s_add_u32 s8, s6, 0x28000
	s_addc_u32 s9, s7, 0
	global_load_dwordx4 v[104:107], v144, s[8:9] sc1 nt
	s_add_u32 s8, s6, 0x2c000
	s_addc_u32 s9, s7, 0
	global_load_dwordx4 v[108:111], v144, s[8:9] sc1 nt
	s_add_u32 s8, s6, 0x30000
	s_addc_u32 s9, s7, 0
	global_load_dwordx4 v[112:115], v144, s[8:9] sc1 nt
	s_add_u32 s8, s6, 0x34000
	s_addc_u32 s9, s7, 0
	global_load_dwordx4 v[116:119], v144, s[8:9] sc1 nt
	s_add_u32 s8, s6, 0x38000
	s_addc_u32 s9, s7, 0
	global_load_dwordx4 v[120:123], v144, s[8:9] sc1 nt
	s_add_u32 s8, s6, 0x3c000
	s_addc_u32 s9, s7, 0
	global_load_dwordx4 v[124:127], v144, s[8:9] sc1 nt
	s_waitcnt vmcnt(16)
	s_add_i32 s1, s11, 0
	s_and_b32 s2, s1, 1
	s_lshl_b32 s2, s2, 7
	s_and_b32 s4, s1, 0xfe
	s_lshr_b32 s4, s4, 1
	s_andn2_b32 s1, s1, 0xff
	s_or_b32 s1, s1, s2
	s_or_b32 s1, s1, s4
	s_lshr_b32 s2, s1, 11
	s_and_b32 s4, s1, 0x7ff
	s_lshr_b32 s5, s4, 7
	s_and_b32 s4, s4, 127
	s_lshl_b32 s12, s2, 23
	s_lshl_b32 s13, s4, 16
	s_add_i32 s12, s12, s13
	s_lshl_b32 s13, s5, 7
	s_add_i32 s12, s12, s13
	s_add_u32 s30, s90, s12
	s_addc_u32 s31, s91, 0
	s_add_u32 s30, s30, 0x4b100000
	s_addc_u32 s31, s31, 0
	s_add_u32 s34, s30, 0x1000
	s_addc_u32 s35, s31, 0
	v_pk_mul_f32 v[0:1], v[0:1], s[36:37] op_sel_hi:[1,0]
	v_pk_mul_f32 v[2:3], v[2:3], s[36:37] op_sel_hi:[1,0]
	v_pk_mul_f32 v[4:5], v[4:5], s[36:37] op_sel_hi:[1,0]
	v_pk_mul_f32 v[6:7], v[6:7], s[36:37] op_sel_hi:[1,0]
	v_pk_mul_f32 v[8:9], v[8:9], s[36:37] op_sel_hi:[1,0]
	v_pk_mul_f32 v[10:11], v[10:11], s[36:37] op_sel_hi:[1,0]
	v_pk_mul_f32 v[12:13], v[12:13], s[36:37] op_sel_hi:[1,0]
	v_pk_mul_f32 v[14:15], v[14:15], s[36:37] op_sel_hi:[1,0]
	v_pk_mul_f32 v[16:17], v[16:17], s[36:37] op_sel_hi:[1,0]
	v_pk_mul_f32 v[18:19], v[18:19], s[36:37] op_sel_hi:[1,0]
	v_pk_mul_f32 v[20:21], v[20:21], s[36:37] op_sel_hi:[1,0]
	v_pk_mul_f32 v[22:23], v[22:23], s[36:37] op_sel_hi:[1,0]
	v_pk_mul_f32 v[24:25], v[24:25], s[36:37] op_sel_hi:[1,0]
	v_pk_mul_f32 v[26:27], v[26:27], s[36:37] op_sel_hi:[1,0]
	v_pk_mul_f32 v[28:29], v[28:29], s[36:37] op_sel_hi:[1,0]
	v_pk_mul_f32 v[30:31], v[30:31], s[36:37] op_sel_hi:[1,0]
	v_pk_mul_f32 v[32:33], v[32:33], s[36:37] op_sel_hi:[1,0]
	v_pk_mul_f32 v[34:35], v[34:35], s[36:37] op_sel_hi:[1,0]
	v_pk_mul_f32 v[36:37], v[36:37], s[36:37] op_sel_hi:[1,0]
	v_pk_mul_f32 v[38:39], v[38:39], s[36:37] op_sel_hi:[1,0]
	v_pk_mul_f32 v[40:41], v[40:41], s[36:37] op_sel_hi:[1,0]
	v_pk_mul_f32 v[42:43], v[42:43], s[36:37] op_sel_hi:[1,0]
	v_pk_mul_f32 v[44:45], v[44:45], s[36:37] op_sel_hi:[1,0]
	v_pk_mul_f32 v[46:47], v[46:47], s[36:37] op_sel_hi:[1,0]
	v_pk_mul_f32 v[48:49], v[48:49], s[36:37] op_sel_hi:[1,0]
	v_pk_mul_f32 v[50:51], v[50:51], s[36:37] op_sel_hi:[1,0]
	v_pk_mul_f32 v[52:53], v[52:53], s[36:37] op_sel_hi:[1,0]
	v_pk_mul_f32 v[54:55], v[54:55], s[36:37] op_sel_hi:[1,0]
	v_pk_mul_f32 v[56:57], v[56:57], s[36:37] op_sel_hi:[1,0]
	v_pk_mul_f32 v[58:59], v[58:59], s[36:37] op_sel_hi:[1,0]
	v_pk_mul_f32 v[60:61], v[60:61], s[36:37] op_sel_hi:[1,0]
	v_pk_mul_f32 v[62:63], v[62:63], s[36:37] op_sel_hi:[1,0]
	v_cvt_pk_fp8_f32 v128, v0, v4
	v_cvt_pk_fp8_f32 v128, v8, v12 op_sel:[0,0,1]
	v_cvt_pk_fp8_f32 v129, v16, v20
	v_cvt_pk_fp8_f32 v129, v24, v28 op_sel:[0,0,1]
	v_cvt_pk_fp8_f32 v130, v32, v36
	v_cvt_pk_fp8_f32 v130, v40, v44 op_sel:[0,0,1]
	v_cvt_pk_fp8_f32 v131, v48, v52
	v_cvt_pk_fp8_f32 v131, v56, v60 op_sel:[0,0,1]
	global_store_dwordx4 v145, v[128:131], s[30:31] sc1 nt
	v_cvt_pk_fp8_f32 v132, v1, v5
	v_cvt_pk_fp8_f32 v132, v9, v13 op_sel:[0,0,1]
	v_cvt_pk_fp8_f32 v133, v17, v21
	v_cvt_pk_fp8_f32 v133, v25, v29 op_sel:[0,0,1]
	v_cvt_pk_fp8_f32 v134, v33, v37
	v_cvt_pk_fp8_f32 v134, v41, v45 op_sel:[0,0,1]
	v_cvt_pk_fp8_f32 v135, v49, v53
	v_cvt_pk_fp8_f32 v135, v57, v61 op_sel:[0,0,1]
	global_store_dwordx4 v145, v[132:135], s[30:31] offset:2048 sc1 nt
	v_cvt_pk_fp8_f32 v136, v2, v6
	v_cvt_pk_fp8_f32 v136, v10, v14 op_sel:[0,0,1]
	v_cvt_pk_fp8_f32 v137, v18, v22
	v_cvt_pk_fp8_f32 v137, v26, v30 op_sel:[0,0,1]
	v_cvt_pk_fp8_f32 v138, v34, v38
	v_cvt_pk_fp8_f32 v138, v42, v46 op_sel:[0,0,1]
	v_cvt_pk_fp8_f32 v139, v50, v54
	v_cvt_pk_fp8_f32 v139, v58, v62 op_sel:[0,0,1]
	global_store_dwordx4 v145, v[136:139], s[34:35] sc1 nt
	v_cvt_pk_fp8_f32 v140, v3, v7
	v_cvt_pk_fp8_f32 v140, v11, v15 op_sel:[0,0,1]
	v_cvt_pk_fp8_f32 v141, v19, v23
	v_cvt_pk_fp8_f32 v141, v27, v31 op_sel:[0,0,1]
	v_cvt_pk_fp8_f32 v142, v35, v39
	v_cvt_pk_fp8_f32 v142, v43, v47 op_sel:[0,0,1]
	v_cvt_pk_fp8_f32 v143, v51, v55
	v_cvt_pk_fp8_f32 v143, v59, v63 op_sel:[0,0,1]
	global_store_dwordx4 v145, v[140:143], s[34:35] offset:2048 sc1 nt
	s_add_i32 s1, s11, 16
	s_and_b32 s2, s1, 1
	s_lshl_b32 s2, s2, 7
	s_and_b32 s4, s1, 0xfe
	s_lshr_b32 s4, s4, 1
	s_andn2_b32 s1, s1, 0xff
	s_or_b32 s1, s1, s2
	s_or_b32 s1, s1, s4
	s_lshr_b32 s2, s1, 11
	s_and_b32 s4, s1, 0x7ff
	s_lshr_b32 s5, s4, 7
	s_and_b32 s4, s4, 127
	s_lshl_b32 s12, s2, 25
	s_lshl_b32 s13, s5, 21
	s_add_i32 s12, s12, s13
	s_lshl_b32 s13, s4, 7
	s_add_i32 s12, s12, s13
	s_add_u32 s6, s66, s12
	s_addc_u32 s7, s67, 0
	global_load_dwordx4 v[0:3], v144, s[6:7] sc1 nt
	s_add_u32 s8, s6, 0x4000
	s_addc_u32 s9, s7, 0
	global_load_dwordx4 v[4:7], v144, s[8:9] sc1 nt
	s_add_u32 s8, s6, 0x8000
	s_addc_u32 s9, s7, 0
	global_load_dwordx4 v[8:11], v144, s[8:9] sc1 nt
	s_add_u32 s8, s6, 0xc000
	s_addc_u32 s9, s7, 0
	global_load_dwordx4 v[12:15], v144, s[8:9] sc1 nt
	s_add_u32 s8, s6, 0x10000
	s_addc_u32 s9, s7, 0
	global_load_dwordx4 v[16:19], v144, s[8:9] sc1 nt
	s_add_u32 s8, s6, 0x14000
	s_addc_u32 s9, s7, 0
	global_load_dwordx4 v[20:23], v144, s[8:9] sc1 nt
	s_add_u32 s8, s6, 0x18000
	s_addc_u32 s9, s7, 0
	global_load_dwordx4 v[24:27], v144, s[8:9] sc1 nt
	s_add_u32 s8, s6, 0x1c000
	s_addc_u32 s9, s7, 0
	global_load_dwordx4 v[28:31], v144, s[8:9] sc1 nt
	s_add_u32 s8, s6, 0x20000
	s_addc_u32 s9, s7, 0
	global_load_dwordx4 v[32:35], v144, s[8:9] sc1 nt
	s_add_u32 s8, s6, 0x24000
	s_addc_u32 s9, s7, 0
	global_load_dwordx4 v[36:39], v144, s[8:9] sc1 nt
	s_add_u32 s8, s6, 0x28000
	s_addc_u32 s9, s7, 0
	global_load_dwordx4 v[40:43], v144, s[8:9] sc1 nt
	s_add_u32 s8, s6, 0x2c000
	s_addc_u32 s9, s7, 0
	global_load_dwordx4 v[44:47], v144, s[8:9] sc1 nt
	s_add_u32 s8, s6, 0x30000
	s_addc_u32 s9, s7, 0
	global_load_dwordx4 v[48:51], v144, s[8:9] sc1 nt
	s_add_u32 s8, s6, 0x34000
	s_addc_u32 s9, s7, 0
	global_load_dwordx4 v[52:55], v144, s[8:9] sc1 nt
	s_add_u32 s8, s6, 0x38000
	s_addc_u32 s9, s7, 0
	global_load_dwordx4 v[56:59], v144, s[8:9] sc1 nt
	s_add_u32 s8, s6, 0x3c000
	s_addc_u32 s9, s7, 0
	global_load_dwordx4 v[60:63], v144, s[8:9] sc1 nt
	s_add_i32 s11, s11, 8
	s_mov_b32 s0, 8
.Lp1s_loop_a:
	s_waitcnt vmcnt(20)
	s_add_i32 s1, s11, 0
	s_and_b32 s2, s1, 1
	s_lshl_b32 s2, s2, 7
	s_and_b32 s4, s1, 0xfe
	s_lshr_b32 s4, s4, 1
	s_andn2_b32 s1, s1, 0xff
	s_or_b32 s1, s1, s2
	s_or_b32 s1, s1, s4
	s_lshr_b32 s2, s1, 11
	s_and_b32 s4, s1, 0x7ff
	s_lshr_b32 s5, s4, 7
	s_and_b32 s4, s4, 127
	s_lshl_b32 s12, s2, 23
	s_lshl_b32 s13, s4, 16
	s_add_i32 s12, s12, s13
	s_lshl_b32 s13, s5, 7
	s_add_i32 s12, s12, s13
	s_add_u32 s30, s90, s12
	s_addc_u32 s31, s91, 0
	s_add_u32 s30, s30, 0x4b100000
	s_addc_u32 s31, s31, 0
	s_add_u32 s34, s30, 0x1000
	s_addc_u32 s35, s31, 0
	v_pk_mul_f32 v[64:65], v[64:65], s[36:37] op_sel_hi:[1,0]
	v_pk_mul_f32 v[66:67], v[66:67], s[36:37] op_sel_hi:[1,0]
	v_pk_mul_f32 v[68:69], v[68:69], s[36:37] op_sel_hi:[1,0]
	v_pk_mul_f32 v[70:71], v[70:71], s[36:37] op_sel_hi:[1,0]
	v_pk_mul_f32 v[72:73], v[72:73], s[36:37] op_sel_hi:[1,0]
	v_pk_mul_f32 v[74:75], v[74:75], s[36:37] op_sel_hi:[1,0]
	v_pk_mul_f32 v[76:77], v[76:77], s[36:37] op_sel_hi:[1,0]
	v_pk_mul_f32 v[78:79], v[78:79], s[36:37] op_sel_hi:[1,0]
	v_pk_mul_f32 v[80:81], v[80:81], s[36:37] op_sel_hi:[1,0]
	v_pk_mul_f32 v[82:83], v[82:83], s[36:37] op_sel_hi:[1,0]
	v_pk_mul_f32 v[84:85], v[84:85], s[36:37] op_sel_hi:[1,0]
	v_pk_mul_f32 v[86:87], v[86:87], s[36:37] op_sel_hi:[1,0]
	v_pk_mul_f32 v[88:89], v[88:89], s[36:37] op_sel_hi:[1,0]
	v_pk_mul_f32 v[90:91], v[90:91], s[36:37] op_sel_hi:[1,0]
	v_pk_mul_f32 v[92:93], v[92:93], s[36:37] op_sel_hi:[1,0]
	v_pk_mul_f32 v[94:95], v[94:95], s[36:37] op_sel_hi:[1,0]
	v_pk_mul_f32 v[96:97], v[96:97], s[36:37] op_sel_hi:[1,0]
	v_pk_mul_f32 v[98:99], v[98:99], s[36:37] op_sel_hi:[1,0]
	v_pk_mul_f32 v[100:101], v[100:101], s[36:37] op_sel_hi:[1,0]
	v_pk_mul_f32 v[102:103], v[102:103], s[36:37] op_sel_hi:[1,0]
	v_pk_mul_f32 v[104:105], v[104:105], s[36:37] op_sel_hi:[1,0]
	v_pk_mul_f32 v[106:107], v[106:107], s[36:37] op_sel_hi:[1,0]
	v_pk_mul_f32 v[108:109], v[108:109], s[36:37] op_sel_hi:[1,0]
	v_pk_mul_f32 v[110:111], v[110:111], s[36:37] op_sel_hi:[1,0]
	v_pk_mul_f32 v[112:113], v[112:113], s[36:37] op_sel_hi:[1,0]
	v_pk_mul_f32 v[114:115], v[114:115], s[36:37] op_sel_hi:[1,0]
	v_pk_mul_f32 v[116:117], v[116:117], s[36:37] op_sel_hi:[1,0]
	v_pk_mul_f32 v[118:119], v[118:119], s[36:37] op_sel_hi:[1,0]
	v_pk_mul_f32 v[120:121], v[120:121], s[36:37] op_sel_hi:[1,0]
	v_pk_mul_f32 v[122:123], v[122:123], s[36:37] op_sel_hi:[1,0]
	v_pk_mul_f32 v[124:125], v[124:125], s[36:37] op_sel_hi:[1,0]
	v_pk_mul_f32 v[126:127], v[126:127], s[36:37] op_sel_hi:[1,0]
	v_cvt_pk_fp8_f32 v128, v64, v68
	v_cvt_pk_fp8_f32 v128, v72, v76 op_sel:[0,0,1]
	v_cvt_pk_fp8_f32 v129, v80, v84
	v_cvt_pk_fp8_f32 v129, v88, v92 op_sel:[0,0,1]
	v_cvt_pk_fp8_f32 v130, v96, v100
	v_cvt_pk_fp8_f32 v130, v104, v108 op_sel:[0,0,1]
	v_cvt_pk_fp8_f32 v131, v112, v116
	v_cvt_pk_fp8_f32 v131, v120, v124 op_sel:[0,0,1]
	global_store_dwordx4 v145, v[128:131], s[30:31] sc1 nt
	v_cvt_pk_fp8_f32 v132, v65, v69
	v_cvt_pk_fp8_f32 v132, v73, v77 op_sel:[0,0,1]
	v_cvt_pk_fp8_f32 v133, v81, v85
	v_cvt_pk_fp8_f32 v133, v89, v93 op_sel:[0,0,1]
	v_cvt_pk_fp8_f32 v134, v97, v101
	v_cvt_pk_fp8_f32 v134, v105, v109 op_sel:[0,0,1]
	v_cvt_pk_fp8_f32 v135, v113, v117
	v_cvt_pk_fp8_f32 v135, v121, v125 op_sel:[0,0,1]
	global_store_dwordx4 v145, v[132:135], s[30:31] offset:2048 sc1 nt
	v_cvt_pk_fp8_f32 v136, v66, v70
	v_cvt_pk_fp8_f32 v136, v74, v78 op_sel:[0,0,1]
	v_cvt_pk_fp8_f32 v137, v82, v86
	v_cvt_pk_fp8_f32 v137, v90, v94 op_sel:[0,0,1]
	v_cvt_pk_fp8_f32 v138, v98, v102
	v_cvt_pk_fp8_f32 v138, v106, v110 op_sel:[0,0,1]
	v_cvt_pk_fp8_f32 v139, v114, v118
	v_cvt_pk_fp8_f32 v139, v122, v126 op_sel:[0,0,1]
	global_store_dwordx4 v145, v[136:139], s[34:35] sc1 nt
	v_cvt_pk_fp8_f32 v140, v67, v71
	v_cvt_pk_fp8_f32 v140, v75, v79 op_sel:[0,0,1]
	v_cvt_pk_fp8_f32 v141, v83, v87
	v_cvt_pk_fp8_f32 v141, v91, v95 op_sel:[0,0,1]
	v_cvt_pk_fp8_f32 v142, v99, v103
	v_cvt_pk_fp8_f32 v142, v107, v111 op_sel:[0,0,1]
	v_cvt_pk_fp8_f32 v143, v115, v119
	v_cvt_pk_fp8_f32 v143, v123, v127 op_sel:[0,0,1]
	global_store_dwordx4 v145, v[140:143], s[34:35] offset:2048 sc1 nt
	s_add_i32 s1, s11, 16
	s_and_b32 s2, s1, 1
	s_lshl_b32 s2, s2, 7
	s_and_b32 s4, s1, 0xfe
	s_lshr_b32 s4, s4, 1
	s_andn2_b32 s1, s1, 0xff
	s_or_b32 s1, s1, s2
	s_or_b32 s1, s1, s4
	s_lshr_b32 s2, s1, 11
	s_and_b32 s4, s1, 0x7ff
	s_lshr_b32 s5, s4, 7
	s_and_b32 s4, s4, 127
	s_lshl_b32 s12, s2, 25
	s_lshl_b32 s13, s5, 21
	s_add_i32 s12, s12, s13
	s_lshl_b32 s13, s4, 7
	s_add_i32 s12, s12, s13
	s_add_u32 s6, s66, s12
	s_addc_u32 s7, s67, 0
	global_load_dwordx4 v[64:67], v144, s[6:7] sc1 nt
	s_add_u32 s8, s6, 0x4000
	s_addc_u32 s9, s7, 0
	global_load_dwordx4 v[68:71], v144, s[8:9] sc1 nt
	s_add_u32 s8, s6, 0x8000
	s_addc_u32 s9, s7, 0
	global_load_dwordx4 v[72:75], v144, s[8:9] sc1 nt
	s_add_u32 s8, s6, 0xc000
	s_addc_u32 s9, s7, 0
	global_load_dwordx4 v[76:79], v144, s[8:9] sc1 nt
	s_add_u32 s8, s6, 0x10000
	s_addc_u32 s9, s7, 0
	global_load_dwordx4 v[80:83], v144, s[8:9] sc1 nt
	s_add_u32 s8, s6, 0x14000
	s_addc_u32 s9, s7, 0
	global_load_dwordx4 v[84:87], v144, s[8:9] sc1 nt
	s_add_u32 s8, s6, 0x18000
	s_addc_u32 s9, s7, 0
	global_load_dwordx4 v[88:91], v144, s[8:9] sc1 nt
	s_add_u32 s8, s6, 0x1c000
	s_addc_u32 s9, s7, 0
	global_load_dwordx4 v[92:95], v144, s[8:9] sc1 nt
	s_add_u32 s8, s6, 0x20000
	s_addc_u32 s9, s7, 0
	global_load_dwordx4 v[96:99], v144, s[8:9] sc1 nt
	s_add_u32 s8, s6, 0x24000
	s_addc_u32 s9, s7, 0
	global_load_dwordx4 v[100:103], v144, s[8:9] sc1 nt
	s_add_u32 s8, s6, 0x28000
	s_addc_u32 s9, s7, 0
	global_load_dwordx4 v[104:107], v144, s[8:9] sc1 nt
	s_add_u32 s8, s6, 0x2c000
	s_addc_u32 s9, s7, 0
	global_load_dwordx4 v[108:111], v144, s[8:9] sc1 nt
	s_add_u32 s8, s6, 0x30000
	s_addc_u32 s9, s7, 0
	global_load_dwordx4 v[112:115], v144, s[8:9] sc1 nt
	s_add_u32 s8, s6, 0x34000
	s_addc_u32 s9, s7, 0
	global_load_dwordx4 v[116:119], v144, s[8:9] sc1 nt
	s_add_u32 s8, s6, 0x38000
	s_addc_u32 s9, s7, 0
	global_load_dwordx4 v[120:123], v144, s[8:9] sc1 nt
	s_add_u32 s8, s6, 0x3c000
	s_addc_u32 s9, s7, 0
	global_load_dwordx4 v[124:127], v144, s[8:9] sc1 nt
	s_waitcnt vmcnt(20)
	s_add_i32 s1, s11, 8
	s_and_b32 s2, s1, 1
	s_lshl_b32 s2, s2, 7
	s_and_b32 s4, s1, 0xfe
	s_lshr_b32 s4, s4, 1
	s_andn2_b32 s1, s1, 0xff
	s_or_b32 s1, s1, s2
	s_or_b32 s1, s1, s4
	s_lshr_b32 s2, s1, 11
	s_and_b32 s4, s1, 0x7ff
	s_lshr_b32 s5, s4, 7
	s_and_b32 s4, s4, 127
	s_lshl_b32 s12, s2, 23
	s_lshl_b32 s13, s4, 16
	s_add_i32 s12, s12, s13
	s_lshl_b32 s13, s5, 7
	s_add_i32 s12, s12, s13
	s_add_u32 s30, s90, s12
	s_addc_u32 s31, s91, 0
	s_add_u32 s30, s30, 0x4b100000
	s_addc_u32 s31, s31, 0
	s_add_u32 s34, s30, 0x1000
	s_addc_u32 s35, s31, 0
	v_pk_mul_f32 v[0:1], v[0:1], s[36:37] op_sel_hi:[1,0]
	v_pk_mul_f32 v[2:3], v[2:3], s[36:37] op_sel_hi:[1,0]
	v_pk_mul_f32 v[4:5], v[4:5], s[36:37] op_sel_hi:[1,0]
	v_pk_mul_f32 v[6:7], v[6:7], s[36:37] op_sel_hi:[1,0]
	v_pk_mul_f32 v[8:9], v[8:9], s[36:37] op_sel_hi:[1,0]
	v_pk_mul_f32 v[10:11], v[10:11], s[36:37] op_sel_hi:[1,0]
	v_pk_mul_f32 v[12:13], v[12:13], s[36:37] op_sel_hi:[1,0]
	v_pk_mul_f32 v[14:15], v[14:15], s[36:37] op_sel_hi:[1,0]
	v_pk_mul_f32 v[16:17], v[16:17], s[36:37] op_sel_hi:[1,0]
	v_pk_mul_f32 v[18:19], v[18:19], s[36:37] op_sel_hi:[1,0]
	v_pk_mul_f32 v[20:21], v[20:21], s[36:37] op_sel_hi:[1,0]
	v_pk_mul_f32 v[22:23], v[22:23], s[36:37] op_sel_hi:[1,0]
	v_pk_mul_f32 v[24:25], v[24:25], s[36:37] op_sel_hi:[1,0]
	v_pk_mul_f32 v[26:27], v[26:27], s[36:37] op_sel_hi:[1,0]
	v_pk_mul_f32 v[28:29], v[28:29], s[36:37] op_sel_hi:[1,0]
	v_pk_mul_f32 v[30:31], v[30:31], s[36:37] op_sel_hi:[1,0]
	v_pk_mul_f32 v[32:33], v[32:33], s[36:37] op_sel_hi:[1,0]
	v_pk_mul_f32 v[34:35], v[34:35], s[36:37] op_sel_hi:[1,0]
	v_pk_mul_f32 v[36:37], v[36:37], s[36:37] op_sel_hi:[1,0]
	v_pk_mul_f32 v[38:39], v[38:39], s[36:37] op_sel_hi:[1,0]
	v_pk_mul_f32 v[40:41], v[40:41], s[36:37] op_sel_hi:[1,0]
	v_pk_mul_f32 v[42:43], v[42:43], s[36:37] op_sel_hi:[1,0]
	v_pk_mul_f32 v[44:45], v[44:45], s[36:37] op_sel_hi:[1,0]
	v_pk_mul_f32 v[46:47], v[46:47], s[36:37] op_sel_hi:[1,0]
	v_pk_mul_f32 v[48:49], v[48:49], s[36:37] op_sel_hi:[1,0]
	v_pk_mul_f32 v[50:51], v[50:51], s[36:37] op_sel_hi:[1,0]
	v_pk_mul_f32 v[52:53], v[52:53], s[36:37] op_sel_hi:[1,0]
	v_pk_mul_f32 v[54:55], v[54:55], s[36:37] op_sel_hi:[1,0]
	v_pk_mul_f32 v[56:57], v[56:57], s[36:37] op_sel_hi:[1,0]
	v_pk_mul_f32 v[58:59], v[58:59], s[36:37] op_sel_hi:[1,0]
	v_pk_mul_f32 v[60:61], v[60:61], s[36:37] op_sel_hi:[1,0]
	v_pk_mul_f32 v[62:63], v[62:63], s[36:37] op_sel_hi:[1,0]
	v_cvt_pk_fp8_f32 v128, v0, v4
	v_cvt_pk_fp8_f32 v128, v8, v12 op_sel:[0,0,1]
	v_cvt_pk_fp8_f32 v129, v16, v20
	v_cvt_pk_fp8_f32 v129, v24, v28 op_sel:[0,0,1]
	v_cvt_pk_fp8_f32 v130, v32, v36
	v_cvt_pk_fp8_f32 v130, v40, v44 op_sel:[0,0,1]
	v_cvt_pk_fp8_f32 v131, v48, v52
	v_cvt_pk_fp8_f32 v131, v56, v60 op_sel:[0,0,1]
	global_store_dwordx4 v145, v[128:131], s[30:31] sc1 nt
	v_cvt_pk_fp8_f32 v132, v1, v5
	v_cvt_pk_fp8_f32 v132, v9, v13 op_sel:[0,0,1]
	v_cvt_pk_fp8_f32 v133, v17, v21
	v_cvt_pk_fp8_f32 v133, v25, v29 op_sel:[0,0,1]
	v_cvt_pk_fp8_f32 v134, v33, v37
	v_cvt_pk_fp8_f32 v134, v41, v45 op_sel:[0,0,1]
	v_cvt_pk_fp8_f32 v135, v49, v53
	v_cvt_pk_fp8_f32 v135, v57, v61 op_sel:[0,0,1]
	global_store_dwordx4 v145, v[132:135], s[30:31] offset:2048 sc1 nt
	v_cvt_pk_fp8_f32 v136, v2, v6
	v_cvt_pk_fp8_f32 v136, v10, v14 op_sel:[0,0,1]
	v_cvt_pk_fp8_f32 v137, v18, v22
	v_cvt_pk_fp8_f32 v137, v26, v30 op_sel:[0,0,1]
	v_cvt_pk_fp8_f32 v138, v34, v38
	v_cvt_pk_fp8_f32 v138, v42, v46 op_sel:[0,0,1]
	v_cvt_pk_fp8_f32 v139, v50, v54
	v_cvt_pk_fp8_f32 v139, v58, v62 op_sel:[0,0,1]
	global_store_dwordx4 v145, v[136:139], s[34:35] sc1 nt
	v_cvt_pk_fp8_f32 v140, v3, v7
	v_cvt_pk_fp8_f32 v140, v11, v15 op_sel:[0,0,1]
	v_cvt_pk_fp8_f32 v141, v19, v23
	v_cvt_pk_fp8_f32 v141, v27, v31 op_sel:[0,0,1]
	v_cvt_pk_fp8_f32 v142, v35, v39
	v_cvt_pk_fp8_f32 v142, v43, v47 op_sel:[0,0,1]
	v_cvt_pk_fp8_f32 v143, v51, v55
	v_cvt_pk_fp8_f32 v143, v59, v63 op_sel:[0,0,1]
	global_store_dwordx4 v145, v[140:143], s[34:35] offset:2048 sc1 nt
	s_add_i32 s1, s11, 24
	s_and_b32 s2, s1, 1
	s_lshl_b32 s2, s2, 7
	s_and_b32 s4, s1, 0xfe
	s_lshr_b32 s4, s4, 1
	s_andn2_b32 s1, s1, 0xff
	s_or_b32 s1, s1, s2
	s_or_b32 s1, s1, s4
	s_lshr_b32 s2, s1, 11
	s_and_b32 s4, s1, 0x7ff
	s_lshr_b32 s5, s4, 7
	s_and_b32 s4, s4, 127
	s_lshl_b32 s12, s2, 25
	s_lshl_b32 s13, s5, 21
	s_add_i32 s12, s12, s13
	s_lshl_b32 s13, s4, 7
	s_add_i32 s12, s12, s13
	s_add_u32 s6, s66, s12
	s_addc_u32 s7, s67, 0
	global_load_dwordx4 v[0:3], v144, s[6:7] sc1 nt
	s_add_u32 s8, s6, 0x4000
	s_addc_u32 s9, s7, 0
	global_load_dwordx4 v[4:7], v144, s[8:9] sc1 nt
	s_add_u32 s8, s6, 0x8000
	s_addc_u32 s9, s7, 0
	global_load_dwordx4 v[8:11], v144, s[8:9] sc1 nt
	s_add_u32 s8, s6, 0xc000
	s_addc_u32 s9, s7, 0
	global_load_dwordx4 v[12:15], v144, s[8:9] sc1 nt
	s_add_u32 s8, s6, 0x10000
	s_addc_u32 s9, s7, 0
	global_load_dwordx4 v[16:19], v144, s[8:9] sc1 nt
	s_add_u32 s8, s6, 0x14000
	s_addc_u32 s9, s7, 0
	global_load_dwordx4 v[20:23], v144, s[8:9] sc1 nt
	s_add_u32 s8, s6, 0x18000
	s_addc_u32 s9, s7, 0
	global_load_dwordx4 v[24:27], v144, s[8:9] sc1 nt
	s_add_u32 s8, s6, 0x1c000
	s_addc_u32 s9, s7, 0
	global_load_dwordx4 v[28:31], v144, s[8:9] sc1 nt
	s_add_u32 s8, s6, 0x20000
	s_addc_u32 s9, s7, 0
	global_load_dwordx4 v[32:35], v144, s[8:9] sc1 nt
	s_add_u32 s8, s6, 0x24000
	s_addc_u32 s9, s7, 0
	global_load_dwordx4 v[36:39], v144, s[8:9] sc1 nt
	s_add_u32 s8, s6, 0x28000
	s_addc_u32 s9, s7, 0
	global_load_dwordx4 v[40:43], v144, s[8:9] sc1 nt
	s_add_u32 s8, s6, 0x2c000
	s_addc_u32 s9, s7, 0
	global_load_dwordx4 v[44:47], v144, s[8:9] sc1 nt
	s_add_u32 s8, s6, 0x30000
	s_addc_u32 s9, s7, 0
	global_load_dwordx4 v[48:51], v144, s[8:9] sc1 nt
	s_add_u32 s8, s6, 0x34000
	s_addc_u32 s9, s7, 0
	global_load_dwordx4 v[52:55], v144, s[8:9] sc1 nt
	s_add_u32 s8, s6, 0x38000
	s_addc_u32 s9, s7, 0
	global_load_dwordx4 v[56:59], v144, s[8:9] sc1 nt
	s_add_u32 s8, s6, 0x3c000
	s_addc_u32 s9, s7, 0
	global_load_dwordx4 v[60:63], v144, s[8:9] sc1 nt
	s_add_i32 s11, s11, 16
	s_sub_i32 s0, s0, 1
	s_cmp_lg_u32 s0, 0
	s_cbranch_scc1 .Lp1s_loop_a
	s_waitcnt vmcnt(20)
	s_add_i32 s1, s11, 0
	s_and_b32 s2, s1, 1
	s_lshl_b32 s2, s2, 7
	s_and_b32 s4, s1, 0xfe
	s_lshr_b32 s4, s4, 1
	s_andn2_b32 s1, s1, 0xff
	s_or_b32 s1, s1, s2
	s_or_b32 s1, s1, s4
	s_lshr_b32 s2, s1, 11
	s_and_b32 s4, s1, 0x7ff
	s_lshr_b32 s5, s4, 7
	s_and_b32 s4, s4, 127
	s_lshl_b32 s12, s2, 23
	s_lshl_b32 s13, s4, 16
	s_add_i32 s12, s12, s13
	s_lshl_b32 s13, s5, 7
	s_add_i32 s12, s12, s13
	s_add_u32 s30, s90, s12
	s_addc_u32 s31, s91, 0
	s_add_u32 s30, s30, 0x4b100000
	s_addc_u32 s31, s31, 0
	s_add_u32 s34, s30, 0x1000
	s_addc_u32 s35, s31, 0
	v_pk_mul_f32 v[64:65], v[64:65], s[36:37] op_sel_hi:[1,0]
	v_pk_mul_f32 v[66:67], v[66:67], s[36:37] op_sel_hi:[1,0]
	v_pk_mul_f32 v[68:69], v[68:69], s[36:37] op_sel_hi:[1,0]
	v_pk_mul_f32 v[70:71], v[70:71], s[36:37] op_sel_hi:[1,0]
	v_pk_mul_f32 v[72:73], v[72:73], s[36:37] op_sel_hi:[1,0]
	v_pk_mul_f32 v[74:75], v[74:75], s[36:37] op_sel_hi:[1,0]
	v_pk_mul_f32 v[76:77], v[76:77], s[36:37] op_sel_hi:[1,0]
	v_pk_mul_f32 v[78:79], v[78:79], s[36:37] op_sel_hi:[1,0]
	v_pk_mul_f32 v[80:81], v[80:81], s[36:37] op_sel_hi:[1,0]
	v_pk_mul_f32 v[82:83], v[82:83], s[36:37] op_sel_hi:[1,0]
	v_pk_mul_f32 v[84:85], v[84:85], s[36:37] op_sel_hi:[1,0]
	v_pk_mul_f32 v[86:87], v[86:87], s[36:37] op_sel_hi:[1,0]
	v_pk_mul_f32 v[88:89], v[88:89], s[36:37] op_sel_hi:[1,0]
	v_pk_mul_f32 v[90:91], v[90:91], s[36:37] op_sel_hi:[1,0]
	v_pk_mul_f32 v[92:93], v[92:93], s[36:37] op_sel_hi:[1,0]
	v_pk_mul_f32 v[94:95], v[94:95], s[36:37] op_sel_hi:[1,0]
	v_pk_mul_f32 v[96:97], v[96:97], s[36:37] op_sel_hi:[1,0]
	v_pk_mul_f32 v[98:99], v[98:99], s[36:37] op_sel_hi:[1,0]
	v_pk_mul_f32 v[100:101], v[100:101], s[36:37] op_sel_hi:[1,0]
	v_pk_mul_f32 v[102:103], v[102:103], s[36:37] op_sel_hi:[1,0]
	v_pk_mul_f32 v[104:105], v[104:105], s[36:37] op_sel_hi:[1,0]
	v_pk_mul_f32 v[106:107], v[106:107], s[36:37] op_sel_hi:[1,0]
	v_pk_mul_f32 v[108:109], v[108:109], s[36:37] op_sel_hi:[1,0]
	v_pk_mul_f32 v[110:111], v[110:111], s[36:37] op_sel_hi:[1,0]
	v_pk_mul_f32 v[112:113], v[112:113], s[36:37] op_sel_hi:[1,0]
	v_pk_mul_f32 v[114:115], v[114:115], s[36:37] op_sel_hi:[1,0]
	v_pk_mul_f32 v[116:117], v[116:117], s[36:37] op_sel_hi:[1,0]
	v_pk_mul_f32 v[118:119], v[118:119], s[36:37] op_sel_hi:[1,0]
	v_pk_mul_f32 v[120:121], v[120:121], s[36:37] op_sel_hi:[1,0]
	v_pk_mul_f32 v[122:123], v[122:123], s[36:37] op_sel_hi:[1,0]
	v_pk_mul_f32 v[124:125], v[124:125], s[36:37] op_sel_hi:[1,0]
	v_pk_mul_f32 v[126:127], v[126:127], s[36:37] op_sel_hi:[1,0]
	v_cvt_pk_fp8_f32 v128, v64, v68
	v_cvt_pk_fp8_f32 v128, v72, v76 op_sel:[0,0,1]
	v_cvt_pk_fp8_f32 v129, v80, v84
	v_cvt_pk_fp8_f32 v129, v88, v92 op_sel:[0,0,1]
	v_cvt_pk_fp8_f32 v130, v96, v100
	v_cvt_pk_fp8_f32 v130, v104, v108 op_sel:[0,0,1]
	v_cvt_pk_fp8_f32 v131, v112, v116
	v_cvt_pk_fp8_f32 v131, v120, v124 op_sel:[0,0,1]
	global_store_dwordx4 v145, v[128:131], s[30:31] sc1 nt
	v_cvt_pk_fp8_f32 v132, v65, v69
	v_cvt_pk_fp8_f32 v132, v73, v77 op_sel:[0,0,1]
	v_cvt_pk_fp8_f32 v133, v81, v85
	v_cvt_pk_fp8_f32 v133, v89, v93 op_sel:[0,0,1]
	v_cvt_pk_fp8_f32 v134, v97, v101
	v_cvt_pk_fp8_f32 v134, v105, v109 op_sel:[0,0,1]
	v_cvt_pk_fp8_f32 v135, v113, v117
	v_cvt_pk_fp8_f32 v135, v121, v125 op_sel:[0,0,1]
	global_store_dwordx4 v145, v[132:135], s[30:31] offset:2048 sc1 nt
	v_cvt_pk_fp8_f32 v136, v66, v70
	v_cvt_pk_fp8_f32 v136, v74, v78 op_sel:[0,0,1]
	v_cvt_pk_fp8_f32 v137, v82, v86
	v_cvt_pk_fp8_f32 v137, v90, v94 op_sel:[0,0,1]
	v_cvt_pk_fp8_f32 v138, v98, v102
	v_cvt_pk_fp8_f32 v138, v106, v110 op_sel:[0,0,1]
	v_cvt_pk_fp8_f32 v139, v114, v118
	v_cvt_pk_fp8_f32 v139, v122, v126 op_sel:[0,0,1]
	global_store_dwordx4 v145, v[136:139], s[34:35] sc1 nt
	v_cvt_pk_fp8_f32 v140, v67, v71
	v_cvt_pk_fp8_f32 v140, v75, v79 op_sel:[0,0,1]
	v_cvt_pk_fp8_f32 v141, v83, v87
	v_cvt_pk_fp8_f32 v141, v91, v95 op_sel:[0,0,1]
	v_cvt_pk_fp8_f32 v142, v99, v103
	v_cvt_pk_fp8_f32 v142, v107, v111 op_sel:[0,0,1]
	v_cvt_pk_fp8_f32 v143, v115, v119
	v_cvt_pk_fp8_f32 v143, v123, v127 op_sel:[0,0,1]
	global_store_dwordx4 v145, v[140:143], s[34:35] offset:2048 sc1 nt
	s_add_i32 s1, s11, 16
	s_and_b32 s2, s1, 1
	s_lshl_b32 s2, s2, 7
	s_and_b32 s4, s1, 0xfe
	s_lshr_b32 s4, s4, 1
	s_andn2_b32 s1, s1, 0xff
	s_or_b32 s1, s1, s2
	s_or_b32 s1, s1, s4
	s_lshr_b32 s2, s1, 11
	s_and_b32 s4, s1, 0x7ff
	s_lshr_b32 s5, s4, 7
	s_and_b32 s4, s4, 127
	s_lshl_b32 s12, s2, 25
	s_lshl_b32 s13, s5, 21
	s_add_i32 s12, s12, s13
	s_lshl_b32 s13, s4, 7
	s_add_i32 s12, s12, s13
	s_add_u32 s6, s66, s12
	s_addc_u32 s7, s67, 0
	global_load_dwordx4 v[64:67], v144, s[6:7] sc1 nt
	s_add_u32 s8, s6, 0x4000
	s_addc_u32 s9, s7, 0
	global_load_dwordx4 v[68:71], v144, s[8:9] sc1 nt
	s_add_u32 s8, s6, 0x8000
	s_addc_u32 s9, s7, 0
	global_load_dwordx4 v[72:75], v144, s[8:9] sc1 nt
	s_add_u32 s8, s6, 0xc000
	s_addc_u32 s9, s7, 0
	global_load_dwordx4 v[76:79], v144, s[8:9] sc1 nt
	s_add_u32 s8, s6, 0x10000
	s_addc_u32 s9, s7, 0
	global_load_dwordx4 v[80:83], v144, s[8:9] sc1 nt
	s_add_u32 s8, s6, 0x14000
	s_addc_u32 s9, s7, 0
	global_load_dwordx4 v[84:87], v144, s[8:9] sc1 nt
	s_add_u32 s8, s6, 0x18000
	s_addc_u32 s9, s7, 0
	global_load_dwordx4 v[88:91], v144, s[8:9] sc1 nt
	s_add_u32 s8, s6, 0x1c000
	s_addc_u32 s9, s7, 0
	global_load_dwordx4 v[92:95], v144, s[8:9] sc1 nt
	s_add_u32 s8, s6, 0x20000
	s_addc_u32 s9, s7, 0
	global_load_dwordx4 v[96:99], v144, s[8:9] sc1 nt
	s_add_u32 s8, s6, 0x24000
	s_addc_u32 s9, s7, 0
	global_load_dwordx4 v[100:103], v144, s[8:9] sc1 nt
	s_add_u32 s8, s6, 0x28000
	s_addc_u32 s9, s7, 0
	global_load_dwordx4 v[104:107], v144, s[8:9] sc1 nt
	s_add_u32 s8, s6, 0x2c000
	s_addc_u32 s9, s7, 0
	global_load_dwordx4 v[108:111], v144, s[8:9] sc1 nt
	s_add_u32 s8, s6, 0x30000
	s_addc_u32 s9, s7, 0
	global_load_dwordx4 v[112:115], v144, s[8:9] sc1 nt
	s_add_u32 s8, s6, 0x34000
	s_addc_u32 s9, s7, 0
	global_load_dwordx4 v[116:119], v144, s[8:9] sc1 nt
	s_add_u32 s8, s6, 0x38000
	s_addc_u32 s9, s7, 0
	global_load_dwordx4 v[120:123], v144, s[8:9] sc1 nt
	s_add_u32 s8, s6, 0x3c000
	s_addc_u32 s9, s7, 0
	global_load_dwordx4 v[124:127], v144, s[8:9] sc1 nt
	s_waitcnt vmcnt(20)
	s_add_i32 s1, s11, 8
	s_and_b32 s2, s1, 1
	s_lshl_b32 s2, s2, 7
	s_and_b32 s4, s1, 0xfe
	s_lshr_b32 s4, s4, 1
	s_andn2_b32 s1, s1, 0xff
	s_or_b32 s1, s1, s2
	s_or_b32 s1, s1, s4
	s_lshr_b32 s2, s1, 11
	s_and_b32 s4, s1, 0x7ff
	s_lshr_b32 s5, s4, 7
	s_and_b32 s4, s4, 127
	s_lshl_b32 s12, s2, 23
	s_lshl_b32 s13, s4, 16
	s_add_i32 s12, s12, s13
	s_lshl_b32 s13, s5, 7
	s_add_i32 s12, s12, s13
	s_add_u32 s30, s90, s12
	s_addc_u32 s31, s91, 0
	s_add_u32 s30, s30, 0x4b100000
	s_addc_u32 s31, s31, 0
	s_add_u32 s34, s30, 0x1000
	s_addc_u32 s35, s31, 0
	v_pk_mul_f32 v[0:1], v[0:1], s[36:37] op_sel_hi:[1,0]
	v_pk_mul_f32 v[2:3], v[2:3], s[36:37] op_sel_hi:[1,0]
	v_pk_mul_f32 v[4:5], v[4:5], s[36:37] op_sel_hi:[1,0]
	v_pk_mul_f32 v[6:7], v[6:7], s[36:37] op_sel_hi:[1,0]
	v_pk_mul_f32 v[8:9], v[8:9], s[36:37] op_sel_hi:[1,0]
	v_pk_mul_f32 v[10:11], v[10:11], s[36:37] op_sel_hi:[1,0]
	v_pk_mul_f32 v[12:13], v[12:13], s[36:37] op_sel_hi:[1,0]
	v_pk_mul_f32 v[14:15], v[14:15], s[36:37] op_sel_hi:[1,0]
	v_pk_mul_f32 v[16:17], v[16:17], s[36:37] op_sel_hi:[1,0]
	v_pk_mul_f32 v[18:19], v[18:19], s[36:37] op_sel_hi:[1,0]
	v_pk_mul_f32 v[20:21], v[20:21], s[36:37] op_sel_hi:[1,0]
	v_pk_mul_f32 v[22:23], v[22:23], s[36:37] op_sel_hi:[1,0]
	v_pk_mul_f32 v[24:25], v[24:25], s[36:37] op_sel_hi:[1,0]
	v_pk_mul_f32 v[26:27], v[26:27], s[36:37] op_sel_hi:[1,0]
	v_pk_mul_f32 v[28:29], v[28:29], s[36:37] op_sel_hi:[1,0]
	v_pk_mul_f32 v[30:31], v[30:31], s[36:37] op_sel_hi:[1,0]
	v_pk_mul_f32 v[32:33], v[32:33], s[36:37] op_sel_hi:[1,0]
	v_pk_mul_f32 v[34:35], v[34:35], s[36:37] op_sel_hi:[1,0]
	v_pk_mul_f32 v[36:37], v[36:37], s[36:37] op_sel_hi:[1,0]
	v_pk_mul_f32 v[38:39], v[38:39], s[36:37] op_sel_hi:[1,0]
	v_pk_mul_f32 v[40:41], v[40:41], s[36:37] op_sel_hi:[1,0]
	v_pk_mul_f32 v[42:43], v[42:43], s[36:37] op_sel_hi:[1,0]
	v_pk_mul_f32 v[44:45], v[44:45], s[36:37] op_sel_hi:[1,0]
	v_pk_mul_f32 v[46:47], v[46:47], s[36:37] op_sel_hi:[1,0]
	v_pk_mul_f32 v[48:49], v[48:49], s[36:37] op_sel_hi:[1,0]
	v_pk_mul_f32 v[50:51], v[50:51], s[36:37] op_sel_hi:[1,0]
	v_pk_mul_f32 v[52:53], v[52:53], s[36:37] op_sel_hi:[1,0]
	v_pk_mul_f32 v[54:55], v[54:55], s[36:37] op_sel_hi:[1,0]
	v_pk_mul_f32 v[56:57], v[56:57], s[36:37] op_sel_hi:[1,0]
	v_pk_mul_f32 v[58:59], v[58:59], s[36:37] op_sel_hi:[1,0]
	v_pk_mul_f32 v[60:61], v[60:61], s[36:37] op_sel_hi:[1,0]
	v_pk_mul_f32 v[62:63], v[62:63], s[36:37] op_sel_hi:[1,0]
	v_cvt_pk_fp8_f32 v128, v0, v4
	v_cvt_pk_fp8_f32 v128, v8, v12 op_sel:[0,0,1]
	v_cvt_pk_fp8_f32 v129, v16, v20
	v_cvt_pk_fp8_f32 v129, v24, v28 op_sel:[0,0,1]
	v_cvt_pk_fp8_f32 v130, v32, v36
	v_cvt_pk_fp8_f32 v130, v40, v44 op_sel:[0,0,1]
	v_cvt_pk_fp8_f32 v131, v48, v52
	v_cvt_pk_fp8_f32 v131, v56, v60 op_sel:[0,0,1]
	global_store_dwordx4 v145, v[128:131], s[30:31] sc1 nt
	v_cvt_pk_fp8_f32 v132, v1, v5
	v_cvt_pk_fp8_f32 v132, v9, v13 op_sel:[0,0,1]
	v_cvt_pk_fp8_f32 v133, v17, v21
	v_cvt_pk_fp8_f32 v133, v25, v29 op_sel:[0,0,1]
	v_cvt_pk_fp8_f32 v134, v33, v37
	v_cvt_pk_fp8_f32 v134, v41, v45 op_sel:[0,0,1]
	v_cvt_pk_fp8_f32 v135, v49, v53
	v_cvt_pk_fp8_f32 v135, v57, v61 op_sel:[0,0,1]
	global_store_dwordx4 v145, v[132:135], s[30:31] offset:2048 sc1 nt
	v_cvt_pk_fp8_f32 v136, v2, v6
	v_cvt_pk_fp8_f32 v136, v10, v14 op_sel:[0,0,1]
	v_cvt_pk_fp8_f32 v137, v18, v22
	v_cvt_pk_fp8_f32 v137, v26, v30 op_sel:[0,0,1]
	v_cvt_pk_fp8_f32 v138, v34, v38
	v_cvt_pk_fp8_f32 v138, v42, v46 op_sel:[0,0,1]
	v_cvt_pk_fp8_f32 v139, v50, v54
	v_cvt_pk_fp8_f32 v139, v58, v62 op_sel:[0,0,1]
	global_store_dwordx4 v145, v[136:139], s[34:35] sc1 nt
	v_cvt_pk_fp8_f32 v140, v3, v7
	v_cvt_pk_fp8_f32 v140, v11, v15 op_sel:[0,0,1]
	v_cvt_pk_fp8_f32 v141, v19, v23
	v_cvt_pk_fp8_f32 v141, v27, v31 op_sel:[0,0,1]
	v_cvt_pk_fp8_f32 v142, v35, v39
	v_cvt_pk_fp8_f32 v142, v43, v47 op_sel:[0,0,1]
	v_cvt_pk_fp8_f32 v143, v51, v55
	v_cvt_pk_fp8_f32 v143, v59, v63 op_sel:[0,0,1]
	global_store_dwordx4 v145, v[140:143], s[34:35] offset:2048 sc1 nt
	s_waitcnt vmcnt(4)
	s_add_i32 s1, s11, 16
	s_and_b32 s2, s1, 1
	s_lshl_b32 s2, s2, 7
	s_and_b32 s4, s1, 0xfe
	s_lshr_b32 s4, s4, 1
	s_andn2_b32 s1, s1, 0xff
	s_or_b32 s1, s1, s2
	s_or_b32 s1, s1, s4
	s_lshr_b32 s2, s1, 11
	s_and_b32 s4, s1, 0x7ff
	s_lshr_b32 s5, s4, 7
	s_and_b32 s4, s4, 127
	s_lshl_b32 s12, s2, 23
	s_lshl_b32 s13, s4, 16
	s_add_i32 s12, s12, s13
	s_lshl_b32 s13, s5, 7
	s_add_i32 s12, s12, s13
	s_add_u32 s30, s90, s12
	s_addc_u32 s31, s91, 0
	s_add_u32 s30, s30, 0x4b100000
	s_addc_u32 s31, s31, 0
	s_add_u32 s34, s30, 0x1000
	s_addc_u32 s35, s31, 0
	v_pk_mul_f32 v[64:65], v[64:65], s[36:37] op_sel_hi:[1,0]
	v_pk_mul_f32 v[66:67], v[66:67], s[36:37] op_sel_hi:[1,0]
	v_pk_mul_f32 v[68:69], v[68:69], s[36:37] op_sel_hi:[1,0]
	v_pk_mul_f32 v[70:71], v[70:71], s[36:37] op_sel_hi:[1,0]
	v_pk_mul_f32 v[72:73], v[72:73], s[36:37] op_sel_hi:[1,0]
	v_pk_mul_f32 v[74:75], v[74:75], s[36:37] op_sel_hi:[1,0]
	v_pk_mul_f32 v[76:77], v[76:77], s[36:37] op_sel_hi:[1,0]
	v_pk_mul_f32 v[78:79], v[78:79], s[36:37] op_sel_hi:[1,0]
	v_pk_mul_f32 v[80:81], v[80:81], s[36:37] op_sel_hi:[1,0]
	v_pk_mul_f32 v[82:83], v[82:83], s[36:37] op_sel_hi:[1,0]
	v_pk_mul_f32 v[84:85], v[84:85], s[36:37] op_sel_hi:[1,0]
	v_pk_mul_f32 v[86:87], v[86:87], s[36:37] op_sel_hi:[1,0]
	v_pk_mul_f32 v[88:89], v[88:89], s[36:37] op_sel_hi:[1,0]
	v_pk_mul_f32 v[90:91], v[90:91], s[36:37] op_sel_hi:[1,0]
	v_pk_mul_f32 v[92:93], v[92:93], s[36:37] op_sel_hi:[1,0]
	v_pk_mul_f32 v[94:95], v[94:95], s[36:37] op_sel_hi:[1,0]
	v_pk_mul_f32 v[96:97], v[96:97], s[36:37] op_sel_hi:[1,0]
	v_pk_mul_f32 v[98:99], v[98:99], s[36:37] op_sel_hi:[1,0]
	v_pk_mul_f32 v[100:101], v[100:101], s[36:37] op_sel_hi:[1,0]
	v_pk_mul_f32 v[102:103], v[102:103], s[36:37] op_sel_hi:[1,0]
	v_pk_mul_f32 v[104:105], v[104:105], s[36:37] op_sel_hi:[1,0]
	v_pk_mul_f32 v[106:107], v[106:107], s[36:37] op_sel_hi:[1,0]
	v_pk_mul_f32 v[108:109], v[108:109], s[36:37] op_sel_hi:[1,0]
	v_pk_mul_f32 v[110:111], v[110:111], s[36:37] op_sel_hi:[1,0]
	v_pk_mul_f32 v[112:113], v[112:113], s[36:37] op_sel_hi:[1,0]
	v_pk_mul_f32 v[114:115], v[114:115], s[36:37] op_sel_hi:[1,0]
	v_pk_mul_f32 v[116:117], v[116:117], s[36:37] op_sel_hi:[1,0]
	v_pk_mul_f32 v[118:119], v[118:119], s[36:37] op_sel_hi:[1,0]
	v_pk_mul_f32 v[120:121], v[120:121], s[36:37] op_sel_hi:[1,0]
	v_pk_mul_f32 v[122:123], v[122:123], s[36:37] op_sel_hi:[1,0]
	v_pk_mul_f32 v[124:125], v[124:125], s[36:37] op_sel_hi:[1,0]
	v_pk_mul_f32 v[126:127], v[126:127], s[36:37] op_sel_hi:[1,0]
	v_cvt_pk_fp8_f32 v128, v64, v68
	v_cvt_pk_fp8_f32 v128, v72, v76 op_sel:[0,0,1]
	v_cvt_pk_fp8_f32 v129, v80, v84
	v_cvt_pk_fp8_f32 v129, v88, v92 op_sel:[0,0,1]
	v_cvt_pk_fp8_f32 v130, v96, v100
	v_cvt_pk_fp8_f32 v130, v104, v108 op_sel:[0,0,1]
	v_cvt_pk_fp8_f32 v131, v112, v116
	v_cvt_pk_fp8_f32 v131, v120, v124 op_sel:[0,0,1]
	global_store_dwordx4 v145, v[128:131], s[30:31] sc1 nt
	v_cvt_pk_fp8_f32 v132, v65, v69
	v_cvt_pk_fp8_f32 v132, v73, v77 op_sel:[0,0,1]
	v_cvt_pk_fp8_f32 v133, v81, v85
	v_cvt_pk_fp8_f32 v133, v89, v93 op_sel:[0,0,1]
	v_cvt_pk_fp8_f32 v134, v97, v101
	v_cvt_pk_fp8_f32 v134, v105, v109 op_sel:[0,0,1]
	v_cvt_pk_fp8_f32 v135, v113, v117
	v_cvt_pk_fp8_f32 v135, v121, v125 op_sel:[0,0,1]
	global_store_dwordx4 v145, v[132:135], s[30:31] offset:2048 sc1 nt
	v_cvt_pk_fp8_f32 v136, v66, v70
	v_cvt_pk_fp8_f32 v136, v74, v78 op_sel:[0,0,1]
	v_cvt_pk_fp8_f32 v137, v82, v86
	v_cvt_pk_fp8_f32 v137, v90, v94 op_sel:[0,0,1]
	v_cvt_pk_fp8_f32 v138, v98, v102
	v_cvt_pk_fp8_f32 v138, v106, v110 op_sel:[0,0,1]
	v_cvt_pk_fp8_f32 v139, v114, v118
	v_cvt_pk_fp8_f32 v139, v122, v126 op_sel:[0,0,1]
	global_store_dwordx4 v145, v[136:139], s[34:35] sc1 nt
	v_cvt_pk_fp8_f32 v140, v67, v71
	v_cvt_pk_fp8_f32 v140, v75, v79 op_sel:[0,0,1]
	v_cvt_pk_fp8_f32 v141, v83, v87
	v_cvt_pk_fp8_f32 v141, v91, v95 op_sel:[0,0,1]
	v_cvt_pk_fp8_f32 v142, v99, v103
	v_cvt_pk_fp8_f32 v142, v107, v111 op_sel:[0,0,1]
	v_cvt_pk_fp8_f32 v143, v115, v119
	v_cvt_pk_fp8_f32 v143, v123, v127 op_sel:[0,0,1]
	global_store_dwordx4 v145, v[140:143], s[34:35] offset:2048 sc1 nt
	s_waitcnt vmcnt(0)
